# combine+LN2 phase: all 16 gamma/beta quads loaded before the LN reductions into free registers, next token's slots/weights prefetched with 4 dwordx4 loads in the tail, x1 chunk 0 renamed so the loop-t
# speedup vs baseline: 1.0041x; 1.0041x over previous
.LBB0_1351:
	v_readlane_b32 s4, v254, 47
	v_readlane_b32 s5, v254, 48
	v_readlane_b32 s8, v252, 1
	s_xor_b64 s[40:41], s[4:5], -1
	v_readlane_b32 s10, v252, 3
	s_cmp_le_i32 s10, s12
	s_cselect_b64 s[4:5], -1, 0
	s_and_b64 s[42:43], s[4:5], s[6:7]
	s_andn2_b64 vcc, exec, s[42:43]
	v_readlane_b32 s9, v252, 2
	v_readlane_b32 s11, v252, 4
	s_cbranch_vccnz .LBB0_1371
	v_mbcnt_lo_u32_b32 v61, -1, 0
	v_mbcnt_hi_u32_b32 v61, -1, v61
	v_readlane_b32 s27, v252, 0
	s_lshl_b32 s4, s27, 3
	v_readlane_b32 s5, v252, 5
	v_readlane_b32 s38, v252, 6
	s_add_i32 s44, s4, s5
	v_readlane_b32 s39, v252, 7
	s_cmpk_gt_i32 s44, 0x3fff
	s_cbranch_scc1 .LBB0_1371
	s_load_dwordx8 s[4:11], s[38:39], 0xc8
	v_readlane_b32 s38, v254, 47
	v_readlane_b32 s39, v254, 48
	s_waitcnt lgkmcnt(0)
	s_add_u32 s46, s10, 0x2a200000
	s_addc_u32 s47, s11, 0
	s_add_u32 s12, s10, 0x240000
	s_addc_u32 s18, s11, 0
	s_add_u32 s20, s10, 0x140000
	s_addc_u32 s21, s11, 0
	s_add_u32 s30, s10, 0x22200000
	s_addc_u32 s45, s11, 0
	s_and_b64 s[38:39], s[38:39], exec
	s_cselect_b32 s9, s45, s9
	s_cselect_b32 s8, s30, s8
	s_lshl_b32 s30, s74, 11
	s_lshl_b64 s[38:39], s[30:31], 2
	s_add_u32 s4, s4, s38
	s_addc_u32 s5, s5, s39
	s_add_u32 s6, s6, s38
	s_addc_u32 s7, s7, s39
	s_ashr_i32 s45, s44, 31
	s_lshl_b32 s27, s27, 6
	v_readlane_b32 s30, v254, 30
	s_lshl_b64 s[48:49], s[44:45], 11
	s_add_i32 s50, s30, s27
	s_lshl_b64 s[52:53], s[44:45], 12
	s_lshl_b64 s[54:55], s[44:45], 13
	s_add_i32 s100, s50, -7
	s_lshl_b32 s100, s100, 2
	v_mov_b32_e32 v60, s100
	v_add_u32_e32 v94, 0x100000, v60
	global_load_dwordx4 v[194:197], v94, s[20:21]
	global_load_dwordx4 v[198:201], v94, s[20:21] offset:16
	global_load_dwordx4 v[202:205], v60, s[20:21]
	global_load_dwordx4 v[206:209], v60, s[20:21] offset:16
	s_waitcnt vmcnt(0)
	s_branch .LBB0_1355

.LBB0_1355:
	v_mov_b32_e32 v23, v61
	v_lshlrev_b32_e32 v0, 4, v23
	v_lshl_add_u64 v[10:11], s[52:53], 0, v[0:1]
	v_lshl_add_u64 v[2:3], s[10:11], 0, v[10:11]
	v_add_co_u32_e32 v12, vcc, s26, v2
	s_nop 1
	v_addc_co_u32_e32 v13, vcc, 0, v3, vcc
	global_load_dwordx4 v[240:243], v[12:13], off
	s_add_i32 s38, s44, 0x24000
	s_ashr_i32 s39, s38, 31
	s_lshl_b64 s[38:39], s[38:39], 11
	s_waitcnt vmcnt(9)
	v_lshlrev_b32_e32 v36, 3, v23
	s_add_u32 s38, s46, s38
	s_addc_u32 s39, s47, s39
	v_mov_b32_e32 v0, v36
	v_lshl_add_u64 v[18:19], s[46:47], 0, v[0:1]
	global_load_dwordx2 v[16:17], v36, s[38:39]
	s_mov_b32 s30, 0x3d800000
	s_mov_b64 s[58:59], -1
	v_readfirstlane_b32 s56, v194
	s_ashr_i32 s57, s56, 31
	s_lshl_b64 s[56:57], s[56:57], 11
	v_lshl_add_u64 v[20:21], v[18:19], 0, s[56:57]
	global_load_dwordx2 v[14:15], v[20:21], off
	global_load_dwordx4 v[6:9], v[12:13], off offset:1024
	global_load_dwordx2 v[30:31], v36, s[38:39] offset:512
	global_load_dwordx2 v[64:65], v36, s[38:39] offset:1024
	global_load_dwordx2 v[54:55], v36, s[38:39] offset:1536
	v_readfirstlane_b32 s38, v195
	s_ashr_i32 s39, s38, 31
	s_lshl_b64 s[38:39], s[38:39], 11
	v_lshl_add_u64 v[40:41], v[18:19], 0, s[38:39]
	global_load_dwordx2 v[42:43], v[40:41], off
	v_readfirstlane_b32 s27, v202
	v_readfirstlane_b32 s38, v196
	s_ashr_i32 s39, s38, 31
	s_lshl_b64 s[38:39], s[38:39], 11
	v_lshl_add_u64 v[46:47], v[18:19], 0, s[38:39]
	v_readfirstlane_b32 s38, v197
	s_ashr_i32 s39, s38, 31
	s_lshl_b64 s[38:39], s[38:39], 11
	v_lshl_add_u64 v[50:51], v[18:19], 0, s[38:39]
	global_load_dwordx2 v[48:49], v[46:47], off
	global_load_dwordx2 v[58:59], v[50:51], off
	global_load_dwordx2 v[102:103], v[20:21], off offset:512
	global_load_dwordx2 v[160:161], v[20:21], off offset:1024
	v_mul_f32_e32 v60, s27, v239
	v_readfirstlane_b32 s38, v198
	s_ashr_i32 s39, s38, 31
	s_lshl_b64 s[38:39], s[38:39], 11
	v_lshl_add_u64 v[62:63], v[18:19], 0, s[38:39]
	global_load_dwordx2 v[68:69], v[62:63], off
	global_load_dwordx2 v[96:97], v[20:21], off offset:1536
	v_readfirstlane_b32 s27, v203
	v_readfirstlane_b32 s38, v199
	s_ashr_i32 s39, s38, 31
	s_lshl_b64 s[38:39], s[38:39], 11
	v_lshl_add_u64 v[72:73], v[18:19], 0, s[38:39]
	global_load_dwordx2 v[74:75], v[72:73], off
	v_mul_f32_e32 v2, s27, v239
	v_readfirstlane_b32 s27, v204
	v_readfirstlane_b32 s38, v200
	s_ashr_i32 s39, s38, 31
	s_lshl_b64 s[38:39], s[38:39], 11
	v_lshl_add_u64 v[80:81], v[18:19], 0, s[38:39]
	global_load_dwordx2 v[90:91], v[80:81], off
	v_readfirstlane_b32 s38, v201
	s_ashr_i32 s39, s38, 31
	s_lshl_b64 s[38:39], s[38:39], 11
	v_lshl_add_u64 v[94:95], v[18:19], 0, s[38:39]
	global_load_dwordx2 v[110:111], v[94:95], off
	global_load_dwordx2 v[114:115], v[40:41], off offset:512
	global_load_dwordx2 v[120:121], v[46:47], off offset:512
	global_load_dwordx2 v[182:183], v[40:41], off offset:1024
	global_load_dwordx2 v[98:99], v[40:41], off offset:1536
	global_load_dwordx2 v[126:127], v[50:51], off offset:512
	global_load_dwordx2 v[134:135], v[62:63], off offset:512
	global_load_dwordx2 v[184:185], v[46:47], off offset:1024
	global_load_dwordx2 v[100:101], v[46:47], off offset:1536
	global_load_dwordx2 v[144:145], v[72:73], off offset:512
	global_load_dwordx2 v[158:159], v[80:81], off offset:512
	global_load_dwordx2 v[186:187], v[50:51], off offset:1024
	global_load_dwordx2 v[106:107], v[50:51], off offset:1536
	global_load_dwordx2 v[188:189], v[94:95], off offset:512
	global_load_dwordx2 v[190:191], v[62:63], off offset:1024
	global_load_dwordx2 v[104:105], v[62:63], off offset:1536
	global_load_dwordx2 v[192:193], v[72:73], off offset:1024
	global_load_dwordx2 v[108:109], v[72:73], off offset:1536
	global_load_dwordx4 v[174:177], v[12:13], off offset:2048
	global_load_dwordx2 v[152:153], v[80:81], off offset:1024
	global_load_dwordx2 v[116:117], v[80:81], off offset:1536
	global_load_dwordx2 v[136:137], v[94:95], off offset:1024
	global_load_dwordx2 v[128:129], v[94:95], off offset:1536
	global_load_dwordx4 v[178:181], v[12:13], off offset:3072
	s_waitcnt vmcnt(38)
	v_lshlrev_b32_e32 v36, 16, v240
	v_and_b32_e32 v37, 0xffff0000, v240
	v_lshlrev_b32_e32 v38, 16, v242
	v_cvt_pk_f32_fp8_e32 v[28:29], v16
	v_cvt_pk_f32_fp8_e32 v[32:33], v17
	v_cvt_pk_f32_fp8_sdwa v[34:35], v16 src0_sel:WORD_1
	v_and_b32_e32 v39, 0xffff0000, v242
	v_mul_f32_e32 v4, s27, v239
	v_readfirstlane_b32 s27, v205
	s_waitcnt vmcnt(33)
	v_cvt_pk_f32_fp8_e32 v[218:219], v54
	v_cvt_pk_f32_fp8_e32 v[224:225], v55
	v_mul_f32_e32 v18, s27, v239
	v_readfirstlane_b32 s27, v206
	v_pk_mul_f32 v[218:219], v[218:219], s[30:31] op_sel_hi:[1,0]
	v_pk_mul_f32 v[224:225], v[224:225], s[30:31] op_sel_hi:[1,0]
	v_mul_f32_e32 v20, s27, v239
	v_readfirstlane_b32 s27, v207
	v_cvt_pk_f32_fp8_sdwa v[52:53], v17 src0_sel:WORD_1
	v_pk_mul_f32 v[16:17], v[28:29], s[30:31] op_sel_hi:[1,0]
	v_mul_f32_e32 v22, s27, v239
	v_readfirstlane_b32 s27, v208
	v_pk_mul_f32 v[28:29], v[32:33], s[30:31] op_sel_hi:[1,0]
	v_pk_mul_f32 v[32:33], v[34:35], s[30:31] op_sel_hi:[1,0]
	v_pk_fma_f32 v[16:17], v[36:37], s[16:17], v[16:17] op_sel_hi:[1,0,1]
	v_cvt_pk_f32_fp8_e32 v[34:35], v14
	v_cvt_pk_f32_fp8_e32 v[36:37], v15
	v_mul_f32_e32 v24, s27, v239
	v_readfirstlane_b32 s27, v209
	v_cvt_pk_f32_fp8_sdwa v[56:57], v14 src0_sel:WORD_1
	v_lshlrev_b32_e32 v44, 16, v241
	v_and_b32_e32 v45, 0xffff0000, v241
	v_pk_fma_f32 v[28:29], v[38:39], s[16:17], v[28:29] op_sel_hi:[1,0,1]
	v_cvt_pk_f32_fp8_sdwa v[14:15], v15 src0_sel:WORD_1
	v_pk_fma_f32 v[38:39], v[60:61], v[34:35], v[16:17] op_sel_hi:[0,1,1]
	v_pk_fma_f32 v[16:17], v[60:61], v[36:37], v[28:29] op_sel_hi:[0,1,1]
	v_pk_fma_f32 v[28:29], v[44:45], s[16:17], v[32:33] op_sel_hi:[1,0,1]
	v_pk_mul_f32 v[32:33], v[52:53], s[30:31] op_sel_hi:[1,0]
	v_pk_fma_f32 v[36:37], v[60:61], v[56:57], v[28:29] op_sel_hi:[0,1,1]
	v_lshlrev_b32_e32 v28, 16, v243
	v_and_b32_e32 v29, 0xffff0000, v243
	v_pk_fma_f32 v[28:29], v[28:29], s[16:17], v[32:33] op_sel_hi:[1,0,1]
	s_waitcnt vmcnt(32)
	v_cvt_pk_f32_fp8_e32 v[56:57], v42
	v_pk_fma_f32 v[14:15], v[60:61], v[14:15], v[28:29] op_sel_hi:[0,1,1]
	v_cvt_pk_f32_fp8_sdwa v[44:45], v42 src0_sel:WORD_1
	v_cvt_pk_f32_fp8_e32 v[32:33], v43
	v_cvt_pk_f32_fp8_sdwa v[28:29], v43 src0_sel:WORD_1
	s_waitcnt vmcnt(31)
	v_cvt_pk_f32_fp8_e32 v[70:71], v48
	v_cvt_pk_f32_fp8_sdwa v[52:53], v48 src0_sel:WORD_1
	s_waitcnt vmcnt(26)
	v_cvt_pk_f32_fp8_e32 v[226:227], v96
	v_cvt_pk_f32_fp8_e32 v[40:41], v49
	v_cvt_pk_f32_fp8_sdwa v[34:35], v49 src0_sel:WORD_1
	v_cvt_pk_f32_fp8_e32 v[78:79], v58
	v_cvt_pk_f32_fp8_sdwa v[66:67], v58 src0_sel:WORD_1
	v_cvt_pk_f32_fp8_e32 v[48:49], v59
	v_cvt_pk_f32_fp8_sdwa v[42:43], v59 src0_sel:WORD_1
	v_cvt_pk_f32_fp8_e32 v[84:85], v68
	v_cvt_pk_f32_fp8_sdwa v[76:77], v68 src0_sel:WORD_1
	v_cvt_pk_f32_fp8_e32 v[58:59], v69
	v_cvt_pk_f32_fp8_sdwa v[46:47], v69 src0_sel:WORD_1
	s_waitcnt vmcnt(25)
	v_cvt_pk_f32_fp8_e32 v[88:89], v74
	v_cvt_pk_f32_fp8_sdwa v[82:83], v74 src0_sel:WORD_1
	v_cvt_pk_f32_fp8_e32 v[68:69], v75
	v_cvt_pk_f32_fp8_sdwa v[50:51], v75 src0_sel:WORD_1
	v_cvt_pk_f32_fp8_sdwa v[112:113], v30 src0_sel:WORD_1
	s_waitcnt vmcnt(24)
	v_cvt_pk_f32_fp8_e32 v[92:93], v90
	v_cvt_pk_f32_fp8_sdwa v[86:87], v90 src0_sel:WORD_1
	v_cvt_pk_f32_fp8_e32 v[74:75], v91
	v_cvt_pk_f32_fp8_sdwa v[62:63], v91 src0_sel:WORD_1
	v_cvt_pk_f32_fp8_e32 v[118:119], v31
	s_waitcnt vmcnt(23)
	v_cvt_pk_f32_fp8_e32 v[94:95], v110
	v_cvt_pk_f32_fp8_sdwa v[90:91], v110 src0_sel:WORD_1
	v_cvt_pk_f32_fp8_e32 v[80:81], v111
	v_cvt_pk_f32_fp8_sdwa v[72:73], v111 src0_sel:WORD_1
	v_cvt_pk_f32_fp8_e32 v[110:111], v30
	v_cvt_pk_f32_fp8_sdwa v[122:123], v31 src0_sel:WORD_1
	s_waitcnt vmcnt(11)
	v_cvt_pk_f32_fp8_e32 v[232:233], v106
	v_cvt_pk_f32_fp8_e32 v[30:31], v102
	v_cvt_pk_f32_fp8_sdwa v[124:125], v102 src0_sel:WORD_1
	v_cvt_pk_f32_fp8_e32 v[130:131], v103
	v_cvt_pk_f32_fp8_sdwa v[132:133], v103 src0_sel:WORD_1
	v_lshlrev_b32_e32 v102, 16, v6
	v_and_b32_e32 v103, 0xffff0000, v6
	s_waitcnt vmcnt(0)
	v_lshlrev_b32_e32 v220, 16, v178
	v_and_b32_e32 v221, 0xffff0000, v178
	v_pk_fma_f32 v[218:219], v[220:221], s[16:17], v[218:219] op_sel_hi:[1,0,1]
	v_cvt_pk_f32_fp8_sdwa v[220:221], v54 src0_sel:WORD_1
	v_pk_fma_f32 v[218:219], v[60:61], v[226:227], v[218:219] op_sel_hi:[0,1,1]
	v_cvt_pk_f32_fp8_e32 v[226:227], v97
	v_cvt_pk_f32_fp8_sdwa v[54:55], v55 src0_sel:WORD_1
	v_lshlrev_b32_e32 v222, 16, v180
	v_and_b32_e32 v223, 0xffff0000, v180
	v_pk_fma_f32 v[222:223], v[222:223], s[16:17], v[224:225] op_sel_hi:[1,0,1]
	v_lshlrev_b32_e32 v180, 16, v181
	v_pk_fma_f32 v[222:223], v[60:61], v[226:227], v[222:223] op_sel_hi:[0,1,1]
	v_cvt_pk_f32_fp8_sdwa v[226:227], v96 src0_sel:WORD_1
	v_cvt_pk_f32_fp8_sdwa v[96:97], v97 src0_sel:WORD_1
	v_and_b32_e32 v181, 0xffff0000, v181
	v_pk_mul_f32 v[54:55], v[54:55], s[30:31] op_sel_hi:[1,0]
	v_pk_mul_f32 v[110:111], v[110:111], s[30:31] op_sel_hi:[1,0]
	v_pk_fma_f32 v[54:55], v[180:181], s[16:17], v[54:55] op_sel_hi:[1,0,1]
	v_cvt_pk_f32_fp8_e32 v[180:181], v98
	v_pk_fma_f32 v[54:55], v[60:61], v[96:97], v[54:55] op_sel_hi:[0,1,1]
	v_cvt_pk_f32_fp8_e32 v[96:97], v100
	v_pk_fma_f32 v[102:103], v[102:103], s[16:17], v[110:111] op_sel_hi:[1,0,1]
	v_pk_fma_f32 v[180:181], v[2:3], v[180:181], v[218:219] op_sel_hi:[0,1,1]
	v_cvt_pk_f32_fp8_e32 v[218:219], v104
	v_pk_fma_f32 v[96:97], v[4:5], v[96:97], v[180:181] op_sel_hi:[0,1,1]
	v_cvt_pk_f32_fp8_e32 v[180:181], v108
	v_pk_fma_f32 v[96:97], v[18:19], v[232:233], v[96:97] op_sel_hi:[0,1,1]
	v_cvt_pk_f32_fp8_e32 v[232:233], v116
	v_pk_fma_f32 v[96:97], v[20:21], v[218:219], v[96:97] op_sel_hi:[0,1,1]
	v_cvt_pk_f32_fp8_e32 v[218:219], v128
	v_pk_fma_f32 v[102:103], v[60:61], v[30:31], v[102:103] op_sel_hi:[0,1,1]
	v_lshlrev_b32_e32 v30, 16, v8
	v_and_b32_e32 v31, 0xffff0000, v8
	v_pk_mul_f32 v[110:111], v[118:119], s[30:31] op_sel_hi:[1,0]
	v_pk_fma_f32 v[96:97], v[22:23], v[180:181], v[96:97] op_sel_hi:[0,1,1]
	v_cvt_pk_f32_fp8_sdwa v[180:181], v98 src0_sel:WORD_1
	v_mul_f32_e32 v26, s27, v239
	v_pk_fma_f32 v[30:31], v[30:31], s[16:17], v[110:111] op_sel_hi:[1,0,1]
	v_lshlrev_b32_e32 v6, 16, v7
	v_and_b32_e32 v7, 0xffff0000, v7
	v_pk_mul_f32 v[110:111], v[112:113], s[30:31] op_sel_hi:[1,0]
	v_lshlrev_b32_e32 v178, 16, v179
	v_and_b32_e32 v179, 0xffff0000, v179
	v_pk_mul_f32 v[220:221], v[220:221], s[30:31] op_sel_hi:[1,0]
	v_pk_fma_f32 v[96:97], v[24:25], v[232:233], v[96:97] op_sel_hi:[0,1,1]
	v_cvt_pk_f32_fp8_sdwa v[232:233], v100 src0_sel:WORD_1
	v_pk_fma_f32 v[6:7], v[6:7], s[16:17], v[110:111] op_sel_hi:[1,0,1]
	v_pk_fma_f32 v[178:179], v[178:179], s[16:17], v[220:221] op_sel_hi:[1,0,1]
	v_pk_fma_f32 v[96:97], v[26:27], v[218:219], v[96:97] op_sel_hi:[0,1,1]
	v_cvt_pk_f32_fp8_sdwa v[218:219], v106 src0_sel:WORD_1
	v_pk_fma_f32 v[110:111], v[60:61], v[124:125], v[6:7] op_sel_hi:[0,1,1]
	v_lshlrev_b32_e32 v6, 16, v9
	v_and_b32_e32 v7, 0xffff0000, v9
	v_pk_mul_f32 v[8:9], v[122:123], s[30:31] op_sel_hi:[1,0]
	v_pk_fma_f32 v[178:179], v[60:61], v[226:227], v[178:179] op_sel_hi:[0,1,1]
	v_pk_fma_f32 v[6:7], v[6:7], s[16:17], v[8:9] op_sel_hi:[1,0,1]
	v_pk_fma_f32 v[178:179], v[2:3], v[180:181], v[178:179] op_sel_hi:[0,1,1]
	v_cvt_pk_f32_fp8_sdwa v[180:181], v104 src0_sel:WORD_1
	v_pk_fma_f32 v[30:31], v[60:61], v[130:131], v[30:31] op_sel_hi:[0,1,1]
	v_pk_fma_f32 v[6:7], v[60:61], v[132:133], v[6:7] op_sel_hi:[0,1,1]
	v_cvt_pk_f32_fp8_e32 v[138:139], v114
	v_cvt_pk_f32_fp8_sdwa v[122:123], v114 src0_sel:WORD_1
	v_cvt_pk_f32_fp8_e32 v[112:113], v115
	v_cvt_pk_f32_fp8_sdwa v[8:9], v115 src0_sel:WORD_1
	v_cvt_pk_f32_fp8_e32 v[146:147], v120
	v_cvt_pk_f32_fp8_sdwa v[130:131], v120 src0_sel:WORD_1
	v_cvt_pk_f32_fp8_e32 v[118:119], v121
	v_cvt_pk_f32_fp8_sdwa v[12:13], v121 src0_sel:WORD_1
	v_cvt_pk_f32_fp8_e32 v[154:155], v126
	v_cvt_pk_f32_fp8_sdwa v[140:141], v126 src0_sel:WORD_1
	v_cvt_pk_f32_fp8_e32 v[124:125], v127
	v_cvt_pk_f32_fp8_sdwa v[114:115], v127 src0_sel:WORD_1
	v_cvt_pk_f32_fp8_e32 v[162:163], v134
	v_cvt_pk_f32_fp8_sdwa v[148:149], v134 src0_sel:WORD_1
	v_cvt_pk_f32_fp8_e32 v[132:133], v135
	v_cvt_pk_f32_fp8_sdwa v[120:121], v135 src0_sel:WORD_1
	v_cvt_pk_f32_fp8_e32 v[166:167], v144
	v_cvt_pk_f32_fp8_sdwa v[156:157], v144 src0_sel:WORD_1
	v_cvt_pk_f32_fp8_e32 v[142:143], v145
	v_cvt_pk_f32_fp8_sdwa v[126:127], v145 src0_sel:WORD_1
	v_cvt_pk_f32_fp8_e32 v[170:171], v158
	v_cvt_pk_f32_fp8_sdwa v[164:165], v158 src0_sel:WORD_1
	v_cvt_pk_f32_fp8_e32 v[150:151], v159
	v_cvt_pk_f32_fp8_sdwa v[134:135], v159 src0_sel:WORD_1
	v_cvt_pk_f32_fp8_e32 v[172:173], v188
	v_cvt_pk_f32_fp8_sdwa v[168:169], v188 src0_sel:WORD_1
	v_cvt_pk_f32_fp8_e32 v[158:159], v189
	v_cvt_pk_f32_fp8_sdwa v[144:145], v189 src0_sel:WORD_1
	v_cvt_pk_f32_fp8_e32 v[188:189], v64
	v_pk_fma_f32 v[178:179], v[4:5], v[232:233], v[178:179] op_sel_hi:[0,1,1]
	v_cvt_pk_f32_fp8_sdwa v[232:233], v108 src0_sel:WORD_1
	v_pk_fma_f32 v[178:179], v[18:19], v[218:219], v[178:179] op_sel_hi:[0,1,1]
	v_cvt_pk_f32_fp8_sdwa v[218:219], v116 src0_sel:WORD_1
	v_cvt_pk_f32_fp8_sdwa v[194:195], v64 src0_sel:WORD_1
	v_cvt_pk_f32_fp8_e32 v[196:197], v65
	v_cvt_pk_f32_fp8_sdwa v[64:65], v65 src0_sel:WORD_1
	v_cvt_pk_f32_fp8_e32 v[198:199], v160
	v_pk_fma_f32 v[178:179], v[20:21], v[180:181], v[178:179] op_sel_hi:[0,1,1]
	v_cvt_pk_f32_fp8_sdwa v[180:181], v128 src0_sel:WORD_1
	v_cvt_pk_f32_fp8_sdwa v[200:201], v160 src0_sel:WORD_1
	v_cvt_pk_f32_fp8_e32 v[202:203], v161
	v_cvt_pk_f32_fp8_sdwa v[160:161], v161 src0_sel:WORD_1
	v_lshlrev_b32_e32 v204, 16, v174
	v_and_b32_e32 v205, 0xffff0000, v174
	v_pk_mul_f32 v[188:189], v[188:189], s[30:31] op_sel_hi:[1,0]
	v_pk_fma_f32 v[178:179], v[22:23], v[232:233], v[178:179] op_sel_hi:[0,1,1]
	v_cvt_pk_f32_fp8_e32 v[232:233], v99
	v_pk_fma_f32 v[188:189], v[204:205], s[16:17], v[188:189] op_sel_hi:[1,0,1]
	v_pk_fma_f32 v[178:179], v[24:25], v[218:219], v[178:179] op_sel_hi:[0,1,1]
	v_cvt_pk_f32_fp8_e32 v[218:219], v101
	v_cvt_pk_f32_fp8_sdwa v[98:99], v99 src0_sel:WORD_1
	v_pk_fma_f32 v[188:189], v[60:61], v[198:199], v[188:189] op_sel_hi:[0,1,1]
	v_lshlrev_b32_e32 v198, 16, v176
	v_and_b32_e32 v199, 0xffff0000, v176
	v_lshlrev_b32_e32 v176, 16, v177
	v_and_b32_e32 v177, 0xffff0000, v177
	v_pk_mul_f32 v[64:65], v[64:65], s[30:31] op_sel_hi:[1,0]
	v_cvt_pk_f32_fp8_sdwa v[100:101], v101 src0_sel:WORD_1
	v_pk_fma_f32 v[64:65], v[176:177], s[16:17], v[64:65] op_sel_hi:[1,0,1]
	v_pk_fma_f32 v[178:179], v[26:27], v[180:181], v[178:179] op_sel_hi:[0,1,1]
	v_cvt_pk_f32_fp8_e32 v[180:181], v107
	v_cvt_pk_f32_fp8_sdwa v[106:107], v107 src0_sel:WORD_1
	v_pk_mul_f32 v[196:197], v[196:197], s[30:31] op_sel_hi:[1,0]
	v_pk_fma_f32 v[64:65], v[60:61], v[160:161], v[64:65] op_sel_hi:[0,1,1]
	v_cvt_pk_f32_fp8_e32 v[160:161], v182
	v_pk_fma_f32 v[222:223], v[2:3], v[232:233], v[222:223] op_sel_hi:[0,1,1]
	v_cvt_pk_f32_fp8_e32 v[232:233], v105
	v_cvt_pk_f32_fp8_sdwa v[104:105], v105 src0_sel:WORD_1
	v_pk_fma_f32 v[196:197], v[198:199], s[16:17], v[196:197] op_sel_hi:[1,0,1]
	v_cvt_pk_f32_fp8_e32 v[198:199], v184
	v_pk_fma_f32 v[218:219], v[4:5], v[218:219], v[222:223] op_sel_hi:[0,1,1]
	v_cvt_pk_f32_fp8_e32 v[222:223], v109
	v_pk_fma_f32 v[54:55], v[2:3], v[98:99], v[54:55] op_sel_hi:[0,1,1]
	v_cvt_pk_f32_fp8_e32 v[204:205], v186
	v_pk_fma_f32 v[54:55], v[4:5], v[100:101], v[54:55] op_sel_hi:[0,1,1]
	v_cvt_pk_f32_fp8_e32 v[212:213], v190
	v_pk_fma_f32 v[180:181], v[18:19], v[180:181], v[218:219] op_sel_hi:[0,1,1]
	v_pk_fma_f32 v[54:55], v[18:19], v[106:107], v[54:55] op_sel_hi:[0,1,1]
	v_cvt_pk_f32_fp8_e32 v[224:225], v192
	v_pk_fma_f32 v[180:181], v[20:21], v[232:233], v[180:181] op_sel_hi:[0,1,1]
	v_pk_fma_f32 v[54:55], v[20:21], v[104:105], v[54:55] op_sel_hi:[0,1,1]
	v_pk_fma_f32 v[104:105], v[2:3], v[160:161], v[188:189] op_sel_hi:[0,1,1]
	v_lshlrev_b32_e32 v174, 16, v175
	v_and_b32_e32 v175, 0xffff0000, v175
	v_pk_mul_f32 v[194:195], v[194:195], s[30:31] op_sel_hi:[1,0]
	v_pk_fma_f32 v[180:181], v[22:23], v[222:223], v[180:181] op_sel_hi:[0,1,1]
	v_cvt_pk_f32_fp8_e32 v[222:223], v152
	v_pk_fma_f32 v[104:105], v[4:5], v[198:199], v[104:105] op_sel_hi:[0,1,1]
	v_pk_fma_f32 v[174:175], v[174:175], s[16:17], v[194:195] op_sel_hi:[1,0,1]
	v_cvt_pk_f32_fp8_sdwa v[176:177], v182 src0_sel:WORD_1
	v_cvt_pk_f32_fp8_e32 v[98:99], v136
	v_pk_fma_f32 v[104:105], v[18:19], v[204:205], v[104:105] op_sel_hi:[0,1,1]
	v_pk_fma_f32 v[174:175], v[60:61], v[200:201], v[174:175] op_sel_hi:[0,1,1]
	v_cvt_pk_f32_fp8_sdwa v[200:201], v184 src0_sel:WORD_1
	v_cvt_pk_f32_fp8_e32 v[218:219], v117
	v_pk_fma_f32 v[104:105], v[20:21], v[212:213], v[104:105] op_sel_hi:[0,1,1]
	v_cvt_pk_f32_fp8_sdwa v[206:207], v186 src0_sel:WORD_1
	v_pk_fma_f32 v[104:105], v[22:23], v[224:225], v[104:105] op_sel_hi:[0,1,1]
	v_cvt_pk_f32_fp8_sdwa v[214:215], v190 src0_sel:WORD_1
	v_pk_fma_f32 v[104:105], v[24:25], v[222:223], v[104:105] op_sel_hi:[0,1,1]
	v_pk_fma_f32 v[6:7], v[2:3], v[8:9], v[6:7] op_sel_hi:[0,1,1]
	v_cvt_pk_f32_fp8_sdwa v[220:221], v192 src0_sel:WORD_1
	v_pk_fma_f32 v[98:99], v[26:27], v[98:99], v[104:105] op_sel_hi:[0,1,1]
	v_pk_fma_f32 v[104:105], v[2:3], v[176:177], v[174:175] op_sel_hi:[0,1,1]
	v_pk_fma_f32 v[6:7], v[4:5], v[12:13], v[6:7] op_sel_hi:[0,1,1]
	v_pk_fma_f32 v[180:181], v[24:25], v[218:219], v[180:181] op_sel_hi:[0,1,1]
	v_cvt_pk_f32_fp8_sdwa v[218:219], v152 src0_sel:WORD_1
	v_pk_fma_f32 v[104:105], v[4:5], v[200:201], v[104:105] op_sel_hi:[0,1,1]
	v_pk_fma_f32 v[6:7], v[18:19], v[114:115], v[6:7] op_sel_hi:[0,1,1]
	v_cvt_pk_f32_fp8_e32 v[194:195], v183
	v_cvt_pk_f32_fp8_sdwa v[100:101], v136 src0_sel:WORD_1
	v_pk_fma_f32 v[104:105], v[18:19], v[206:207], v[104:105] op_sel_hi:[0,1,1]
	v_pk_fma_f32 v[6:7], v[20:21], v[120:121], v[6:7] op_sel_hi:[0,1,1]
	v_pk_fma_f32 v[196:197], v[60:61], v[202:203], v[196:197] op_sel_hi:[0,1,1]
	v_cvt_pk_f32_fp8_e32 v[202:203], v185
	v_cvt_pk_f32_fp8_e32 v[232:233], v129
	v_pk_fma_f32 v[104:105], v[20:21], v[214:215], v[104:105] op_sel_hi:[0,1,1]
	v_pk_fma_f32 v[6:7], v[22:23], v[126:127], v[6:7] op_sel_hi:[0,1,1]
	v_cvt_pk_f32_fp8_e32 v[208:209], v187
	v_pk_fma_f32 v[104:105], v[22:23], v[220:221], v[104:105] op_sel_hi:[0,1,1]
	v_pk_fma_f32 v[6:7], v[24:25], v[134:135], v[6:7] op_sel_hi:[0,1,1]
	v_cvt_pk_f32_fp8_e32 v[216:217], v191
	v_pk_fma_f32 v[104:105], v[24:25], v[218:219], v[104:105] op_sel_hi:[0,1,1]
	v_pk_fma_f32 v[12:13], v[26:27], v[144:145], v[6:7] op_sel_hi:[0,1,1]
	v_pk_fma_f32 v[6:7], v[2:3], v[56:57], v[38:39] op_sel_hi:[0,1,1]
	v_cvt_pk_f32_fp8_e32 v[226:227], v193
	v_pk_fma_f32 v[100:101], v[26:27], v[100:101], v[104:105] op_sel_hi:[0,1,1]
	v_pk_fma_f32 v[104:105], v[2:3], v[194:195], v[196:197] op_sel_hi:[0,1,1]
	v_pk_fma_f32 v[6:7], v[4:5], v[70:71], v[6:7] op_sel_hi:[0,1,1]
	v_pk_fma_f32 v[180:181], v[26:27], v[232:233], v[180:181] op_sel_hi:[0,1,1]
	v_cvt_pk_f32_fp8_e32 v[232:233], v153
	v_pk_fma_f32 v[104:105], v[4:5], v[202:203], v[104:105] op_sel_hi:[0,1,1]
	v_pk_fma_f32 v[6:7], v[18:19], v[78:79], v[6:7] op_sel_hi:[0,1,1]
	v_cvt_pk_f32_fp8_sdwa v[182:183], v183 src0_sel:WORD_1
	v_cvt_pk_f32_fp8_e32 v[106:107], v137
	v_pk_fma_f32 v[104:105], v[18:19], v[208:209], v[104:105] op_sel_hi:[0,1,1]
	v_pk_fma_f32 v[6:7], v[20:21], v[84:85], v[6:7] op_sel_hi:[0,1,1]
	v_pk_fma_f32 v[104:105], v[20:21], v[216:217], v[104:105] op_sel_hi:[0,1,1]
	v_pk_fma_f32 v[6:7], v[22:23], v[88:89], v[6:7] op_sel_hi:[0,1,1]
	v_pk_fma_f32 v[104:105], v[22:23], v[226:227], v[104:105] op_sel_hi:[0,1,1]
	v_pk_fma_f32 v[6:7], v[24:25], v[92:93], v[6:7] op_sel_hi:[0,1,1]
	v_pk_fma_f32 v[104:105], v[24:25], v[232:233], v[104:105] op_sel_hi:[0,1,1]
	v_pk_fma_f32 v[38:39], v[26:27], v[94:95], v[6:7] op_sel_hi:[0,1,1]
	v_pk_fma_f32 v[104:105], v[26:27], v[106:107], v[104:105] op_sel_hi:[0,1,1]
	v_pk_fma_f32 v[64:65], v[2:3], v[182:183], v[64:65] op_sel_hi:[0,1,1]
	v_pk_fma_f32 v[102:103], v[2:3], v[138:139], v[102:103] op_sel_hi:[0,1,1]
	v_pk_fma_f32 v[106:107], v[2:3], v[122:123], v[110:111] op_sel_hi:[0,1,1]
	v_pk_fma_f32 v[30:31], v[2:3], v[112:113], v[30:31] op_sel_hi:[0,1,1]
	v_add_f32_e32 v3, 0, v38
	v_add_f32_e32 v3, v39, v3
	v_pk_fma_f32 v[6:7], v[2:3], v[44:45], v[36:37] op_sel_hi:[0,1,1]
	v_pk_fma_f32 v[6:7], v[4:5], v[52:53], v[6:7] op_sel_hi:[0,1,1]
	v_pk_fma_f32 v[6:7], v[18:19], v[66:67], v[6:7] op_sel_hi:[0,1,1]
	v_pk_fma_f32 v[6:7], v[20:21], v[76:77], v[6:7] op_sel_hi:[0,1,1]
	v_pk_fma_f32 v[6:7], v[22:23], v[82:83], v[6:7] op_sel_hi:[0,1,1]
	v_pk_fma_f32 v[6:7], v[24:25], v[86:87], v[6:7] op_sel_hi:[0,1,1]
	v_pk_fma_f32 v[36:37], v[26:27], v[90:91], v[6:7] op_sel_hi:[0,1,1]
	v_add_f32_e32 v3, v36, v3
	v_add_f32_e32 v3, v37, v3
	v_pk_fma_f32 v[6:7], v[2:3], v[32:33], v[16:17] op_sel_hi:[0,1,1]
	v_pk_fma_f32 v[6:7], v[4:5], v[40:41], v[6:7] op_sel_hi:[0,1,1]
	v_pk_fma_f32 v[6:7], v[18:19], v[48:49], v[6:7] op_sel_hi:[0,1,1]
	v_pk_fma_f32 v[6:7], v[20:21], v[58:59], v[6:7] op_sel_hi:[0,1,1]
	v_cvt_pk_f32_fp8_sdwa v[184:185], v185 src0_sel:WORD_1
	v_pk_fma_f32 v[6:7], v[22:23], v[68:69], v[6:7] op_sel_hi:[0,1,1]
	v_pk_fma_f32 v[6:7], v[24:25], v[74:75], v[6:7] op_sel_hi:[0,1,1]
	v_pk_fma_f32 v[16:17], v[26:27], v[80:81], v[6:7] op_sel_hi:[0,1,1]
	v_add_f32_e32 v3, v16, v3
	v_pk_fma_f32 v[64:65], v[4:5], v[184:185], v[64:65] op_sel_hi:[0,1,1]
	v_pk_fma_f32 v[102:103], v[4:5], v[146:147], v[102:103] op_sel_hi:[0,1,1]
	v_pk_fma_f32 v[106:107], v[4:5], v[130:131], v[106:107] op_sel_hi:[0,1,1]
	v_pk_fma_f32 v[30:31], v[4:5], v[118:119], v[30:31] op_sel_hi:[0,1,1]
	v_add_f32_e32 v5, v17, v3
	v_pk_fma_f32 v[2:3], v[2:3], v[28:29], v[14:15] op_sel_hi:[0,1,1]
	v_pk_fma_f32 v[2:3], v[4:5], v[34:35], v[2:3] op_sel_hi:[0,1,1]
	v_pk_fma_f32 v[2:3], v[18:19], v[42:43], v[2:3] op_sel_hi:[0,1,1]
	v_pk_fma_f32 v[2:3], v[20:21], v[46:47], v[2:3] op_sel_hi:[0,1,1]
	v_pk_fma_f32 v[102:103], v[18:19], v[154:155], v[102:103] op_sel_hi:[0,1,1]
	v_pk_fma_f32 v[2:3], v[22:23], v[50:51], v[2:3] op_sel_hi:[0,1,1]
	v_pk_fma_f32 v[102:103], v[20:21], v[162:163], v[102:103] op_sel_hi:[0,1,1]
	v_pk_fma_f32 v[2:3], v[24:25], v[62:63], v[2:3] op_sel_hi:[0,1,1]
	v_pk_fma_f32 v[102:103], v[22:23], v[166:167], v[102:103] op_sel_hi:[0,1,1]
	v_pk_fma_f32 v[106:107], v[18:19], v[140:141], v[106:107] op_sel_hi:[0,1,1]
	v_pk_fma_f32 v[14:15], v[26:27], v[72:73], v[2:3] op_sel_hi:[0,1,1]
	v_pk_fma_f32 v[102:103], v[24:25], v[170:171], v[102:103] op_sel_hi:[0,1,1]
	v_pk_fma_f32 v[106:107], v[20:21], v[148:149], v[106:107] op_sel_hi:[0,1,1]
	v_add_f32_e32 v2, v14, v5
	v_pk_fma_f32 v[102:103], v[26:27], v[172:173], v[102:103] op_sel_hi:[0,1,1]
	v_pk_fma_f32 v[106:107], v[22:23], v[156:157], v[106:107] op_sel_hi:[0,1,1]
	v_pk_fma_f32 v[30:31], v[18:19], v[124:125], v[30:31] op_sel_hi:[0,1,1]
	v_add_f32_e32 v2, v15, v2
	v_pk_fma_f32 v[106:107], v[24:25], v[164:165], v[106:107] op_sel_hi:[0,1,1]
	v_pk_fma_f32 v[30:31], v[20:21], v[132:133], v[30:31] op_sel_hi:[0,1,1]
	v_add_f32_e32 v2, v2, v102
	v_pk_fma_f32 v[106:107], v[26:27], v[168:169], v[106:107] op_sel_hi:[0,1,1]
	v_pk_fma_f32 v[30:31], v[22:23], v[142:143], v[30:31] op_sel_hi:[0,1,1]
	v_add_f32_e32 v2, v103, v2
	v_pk_fma_f32 v[30:31], v[24:25], v[150:151], v[30:31] op_sel_hi:[0,1,1]
	v_add_f32_e32 v2, v106, v2
	v_pk_fma_f32 v[30:31], v[26:27], v[158:159], v[30:31] op_sel_hi:[0,1,1]
	v_add_f32_e32 v2, v107, v2
	v_add_f32_e32 v2, v30, v2
	v_cvt_pk_f32_fp8_sdwa v[186:187], v187 src0_sel:WORD_1
	v_add_f32_e32 v2, v31, v2
	v_cvt_pk_f32_fp8_sdwa v[190:191], v191 src0_sel:WORD_1
	v_add_f32_e32 v2, v12, v2
	v_cvt_pk_f32_fp8_sdwa v[192:193], v193 src0_sel:WORD_1
	v_add_f32_e32 v2, v13, v2
	v_cvt_pk_f32_fp8_sdwa v[152:153], v153 src0_sel:WORD_1
	v_add_f32_e32 v2, v2, v98
	v_cvt_pk_f32_fp8_sdwa v[136:137], v137 src0_sel:WORD_1
	v_pk_fma_f32 v[64:65], v[18:19], v[186:187], v[64:65] op_sel_hi:[0,1,1]
	v_add_f32_e32 v2, v99, v2
	v_pk_fma_f32 v[64:65], v[20:21], v[190:191], v[64:65] op_sel_hi:[0,1,1]
	v_add_f32_e32 v2, v100, v2
	v_pk_fma_f32 v[64:65], v[22:23], v[192:193], v[64:65] op_sel_hi:[0,1,1]
	v_add_f32_e32 v2, v101, v2
	v_pk_fma_f32 v[64:65], v[24:25], v[152:153], v[64:65] op_sel_hi:[0,1,1]
	v_add_f32_e32 v2, v104, v2
	v_pk_fma_f32 v[64:65], v[26:27], v[136:137], v[64:65] op_sel_hi:[0,1,1]
	v_add_f32_e32 v2, v105, v2
	v_add_f32_e32 v2, v64, v2
	v_cvt_pk_f32_fp8_sdwa v[108:109], v109 src0_sel:WORD_1
	v_add_f32_e32 v2, v65, v2
	v_cvt_pk_f32_fp8_sdwa v[116:117], v117 src0_sel:WORD_1
	v_add_f32_e32 v2, v2, v96
	v_cvt_pk_f32_fp8_sdwa v[128:129], v129 src0_sel:WORD_1
	v_add_f32_e32 v2, v97, v2
	v_add_f32_e32 v2, v178, v2
	v_pk_fma_f32 v[54:55], v[22:23], v[108:109], v[54:55] op_sel_hi:[0,1,1]
	v_add_f32_e32 v2, v179, v2
	v_pk_fma_f32 v[54:55], v[24:25], v[116:117], v[54:55] op_sel_hi:[0,1,1]
	v_add_f32_e32 v2, v180, v2
	v_pk_fma_f32 v[54:55], v[26:27], v[128:129], v[54:55] op_sel_hi:[0,1,1]
	v_add_f32_e32 v2, v181, v2
	v_add_f32_e32 v2, v54, v2
	v_add_f32_e32 v2, v55, v2
	v_lshlrev_b32_e32 v34, 5, v23
	v_readlane_b32 s100, v254, 23
	s_add_i32 s100, s100, s50
	s_add_i32 s100, s100, -7
	s_lshl_b32 s100, s100, 2
	v_mov_b32_e32 v60, s100
	v_add_u32_e32 v94, 0x100000, v60
	v_add_u32_e32 v95, 0x1000, v34
	global_load_dwordx4 v[194:197], v94, s[20:21]
	global_load_dwordx4 v[198:201], v94, s[20:21] offset:16
	global_load_dwordx4 v[202:205], v60, s[20:21]
	global_load_dwordx4 v[206:209], v60, s[20:21] offset:16
	global_load_dwordx4 v[90:93], v34, s[4:5]
	global_load_dwordx4 v[108:111], v34, s[4:5] offset:16
	global_load_dwordx4 v[112:115], v34, s[6:7]
	global_load_dwordx4 v[116:119], v34, s[6:7] offset:16
	global_load_dwordx4 v[120:123], v34, s[4:5] offset:2048
	global_load_dwordx4 v[124:127], v34, s[4:5] offset:2064
	global_load_dwordx4 v[128:131], v34, s[6:7] offset:2048
	global_load_dwordx4 v[132:135], v34, s[6:7] offset:2064
	global_load_dwordx4 v[136:139], v95, s[4:5]
	global_load_dwordx4 v[140:143], v95, s[4:5] offset:16
	global_load_dwordx4 v[144:147], v95, s[6:7]
	global_load_dwordx4 v[148:151], v95, s[6:7] offset:16
	global_load_dwordx4 v[152:155], v95, s[4:5] offset:2048
	global_load_dwordx4 v[156:159], v95, s[4:5] offset:2064
	global_load_dwordx4 v[160:163], v95, s[6:7] offset:2048
	global_load_dwordx4 v[164:167], v95, s[6:7] offset:2064
	ds_swizzle_b32 v3, v2 offset:swizzle(SWAP,1)
	s_add_u32 s56, s8, s54
	v_mov_b32_e32 v35, v1
	s_addc_u32 s57, s9, s55
	s_waitcnt lgkmcnt(0)
	v_add_f32_e32 v2, v2, v3
	ds_swizzle_b32 v3, v2 offset:swizzle(SWAP,2)
	s_waitcnt lgkmcnt(0)
	v_add_f32_e32 v2, v2, v3
	ds_swizzle_b32 v3, v2 offset:swizzle(SWAP,4)
	s_waitcnt lgkmcnt(0)
	v_add_f32_e32 v2, v2, v3
	ds_swizzle_b32 v3, v2 offset:swizzle(SWAP,8)
	s_waitcnt lgkmcnt(0)
	v_add_f32_e32 v18, v2, v3
	ds_swizzle_b32 v19, v18 offset:swizzle(SWAP,16)
	s_waitcnt lgkmcnt(0)
	v_add_f32_e32 v18, v18, v19
	v_mov_b32_e32 v19, v18
	s_nop 1
	v_permlane32_swap_b32_e32 v18, v19
	v_add_f32_e32 v18, v18, v19
	v_mul_f32_e32 v20, 0x3a000000, v18
	v_pk_add_f32 v[22:23], v[38:39], v[20:21] op_sel_hi:[1,0] neg_lo:[0,1] neg_hi:[0,1]
	v_pk_add_f32 v[36:37], v[36:37], v[20:21] op_sel_hi:[1,0] neg_lo:[0,1] neg_hi:[0,1]
	v_pk_mul_f32 v[24:25], v[22:23], v[22:23]
	v_pk_mul_f32 v[56:57], v[36:37], v[36:37]
	v_add_f32_e32 v24, v24, v25
	v_pk_add_f32 v[58:59], v[16:17], v[20:21] op_sel_hi:[1,0] neg_lo:[0,1] neg_hi:[0,1]
	v_add_f32_e32 v24, v56, v24
	v_pk_mul_f32 v[62:63], v[58:59], v[58:59]
	v_add_f32_e32 v24, v57, v24
	v_pk_add_f32 v[66:67], v[14:15], v[20:21] op_sel_hi:[1,0] neg_lo:[0,1] neg_hi:[0,1]
	v_add_f32_e32 v24, v62, v24
	v_pk_mul_f32 v[68:69], v[66:67], v[66:67]
	v_add_f32_e32 v24, v63, v24
	v_pk_add_f32 v[38:39], v[102:103], v[20:21] op_sel_hi:[1,0] neg_lo:[0,1] neg_hi:[0,1]
	v_add_f32_e32 v24, v68, v24
	v_pk_mul_f32 v[70:71], v[38:39], v[38:39]
	v_add_f32_e32 v24, v69, v24
	v_pk_add_f32 v[40:41], v[106:107], v[20:21] op_sel_hi:[1,0] neg_lo:[0,1] neg_hi:[0,1]
	v_add_f32_e32 v24, v70, v24
	v_pk_mul_f32 v[72:73], v[40:41], v[40:41]
	v_add_f32_e32 v24, v71, v24
	v_pk_add_f32 v[42:43], v[30:31], v[20:21] op_sel_hi:[1,0] neg_lo:[0,1] neg_hi:[0,1]
	v_add_f32_e32 v24, v72, v24
	v_pk_mul_f32 v[74:75], v[42:43], v[42:43]
	v_add_f32_e32 v24, v73, v24
	v_pk_add_f32 v[44:45], v[12:13], v[20:21] op_sel_hi:[1,0] neg_lo:[0,1] neg_hi:[0,1]
	v_add_f32_e32 v24, v74, v24
	v_pk_mul_f32 v[76:77], v[44:45], v[44:45]
	v_add_f32_e32 v24, v75, v24
	v_pk_add_f32 v[30:31], v[98:99], v[20:21] op_sel_hi:[1,0] neg_lo:[0,1] neg_hi:[0,1]
	v_add_f32_e32 v24, v76, v24
	v_pk_mul_f32 v[78:79], v[30:31], v[30:31]
	v_add_f32_e32 v24, v77, v24
	v_pk_add_f32 v[32:33], v[100:101], v[20:21] op_sel_hi:[1,0] neg_lo:[0,1] neg_hi:[0,1]
	v_add_f32_e32 v24, v78, v24
	v_pk_mul_f32 v[80:81], v[32:33], v[32:33]
	v_add_f32_e32 v24, v79, v24
	v_pk_add_f32 v[26:27], v[104:105], v[20:21] op_sel_hi:[1,0] neg_lo:[0,1] neg_hi:[0,1]
	v_add_f32_e32 v24, v80, v24
	v_pk_mul_f32 v[82:83], v[26:27], v[26:27]
	v_add_f32_e32 v24, v81, v24
	v_pk_add_f32 v[28:29], v[64:65], v[20:21] op_sel_hi:[1,0] neg_lo:[0,1] neg_hi:[0,1]
	v_add_f32_e32 v24, v82, v24
	v_pk_mul_f32 v[64:65], v[28:29], v[28:29]
	v_add_f32_e32 v24, v83, v24
	v_pk_add_f32 v[16:17], v[96:97], v[20:21] op_sel_hi:[1,0] neg_lo:[0,1] neg_hi:[0,1]
	v_add_f32_e32 v24, v64, v24
	v_pk_mul_f32 v[84:85], v[16:17], v[16:17]
	v_add_f32_e32 v24, v65, v24
	v_pk_add_f32 v[18:19], v[178:179], v[20:21] op_sel_hi:[1,0] neg_lo:[0,1] neg_hi:[0,1]
	v_add_f32_e32 v24, v84, v24
	v_pk_mul_f32 v[86:87], v[18:19], v[18:19]
	v_add_f32_e32 v24, v85, v24
	v_pk_add_f32 v[12:13], v[180:181], v[20:21] op_sel_hi:[1,0] neg_lo:[0,1] neg_hi:[0,1]
	v_add_f32_e32 v24, v86, v24
	v_pk_mul_f32 v[88:89], v[12:13], v[12:13]
	v_add_f32_e32 v24, v87, v24
	v_pk_add_f32 v[14:15], v[54:55], v[20:21] op_sel_hi:[1,0] neg_lo:[0,1] neg_hi:[0,1]
	v_add_f32_e32 v24, v88, v24
	v_pk_mul_f32 v[20:21], v[14:15], v[14:15]
	v_add_f32_e32 v24, v89, v24
	v_add_f32_e32 v20, v20, v24
	v_add_f32_e32 v20, v21, v20
	ds_swizzle_b32 v21, v20 offset:swizzle(SWAP,1)
	s_waitcnt lgkmcnt(0)
	v_add_f32_e32 v20, v20, v21
	ds_swizzle_b32 v21, v20 offset:swizzle(SWAP,2)
	s_waitcnt lgkmcnt(0)
	v_add_f32_e32 v20, v20, v21
	ds_swizzle_b32 v21, v20 offset:swizzle(SWAP,4)
	s_waitcnt lgkmcnt(0)
	v_add_f32_e32 v20, v20, v21
	ds_swizzle_b32 v21, v20 offset:swizzle(SWAP,8)
	s_waitcnt lgkmcnt(0)
	v_add_f32_e32 v20, v20, v21
	ds_swizzle_b32 v21, v20 offset:swizzle(SWAP,16)
	s_waitcnt lgkmcnt(0)
	v_add_f32_e32 v20, v20, v21
	v_mov_b32_e32 v21, v20
	s_nop 1
	v_permlane32_swap_b32_e32 v20, v21
	v_add_f32_e32 v20, v20, v21
	v_fmamk_f32 v20, v20, 0x3a000000, v210
	v_mul_f32_e32 v21, 0x4f800000, v20
	v_cmp_gt_f32_e32 vcc, s25, v20
	s_nop 1
	v_cndmask_b32_e32 v20, v20, v21, vcc
	v_sqrt_f32_e32 v21, v20
	s_nop 0
	v_add_u32_e32 v24, -1, v21
	v_fma_f32 v25, -v24, v21, v20
	v_cmp_ge_f32_e64 s[38:39], 0, v25
	v_add_u32_e32 v25, 1, v21
	s_nop 0
	v_cndmask_b32_e64 v24, v21, v24, s[38:39]
	v_fma_f32 v21, -v25, v21, v20
	v_cmp_lt_f32_e64 s[38:39], 0, v21
	s_nop 1
	v_cndmask_b32_e64 v21, v24, v25, s[38:39]
	v_mul_f32_e32 v24, 0x37800000, v21
	v_cndmask_b32_e32 v21, v21, v24, vcc
	v_cmp_class_f32_e32 vcc, v20, v211
	s_nop 1
	v_cndmask_b32_e32 v24, v21, v20, vcc
	v_div_scale_f32 v25, s[38:39], v24, v24, 1.0
	v_rcp_f32_e32 v54, v25
	v_lshl_add_u64 v[20:21], s[56:57], 0, v[34:35]
	s_add_u32 s56, s10, s48
	s_addc_u32 s57, s11, s49
	v_fma_f32 v55, -v25, v54, 1.0
	v_fmac_f32_e32 v54, v55, v54
	v_div_scale_f32 v55, vcc, 1.0, v24, 1.0
	v_mul_f32_e32 v56, v55, v54
	v_fma_f32 v57, -v25, v56, v55
	v_fmac_f32_e32 v56, v57, v54
	v_fma_f32 v25, -v25, v56, v55
	v_div_fmas_f32 v25, v25, v54, v56
	v_div_fixup_f32 v24, v25, v24, 1.0
	v_pk_mul_f32 v[22:23], v[22:23], v[24:25] op_sel_hi:[1,0]
	s_andn2_b64 vcc, exec, s[40:41]
	s_waitcnt vmcnt(12)
	v_pk_fma_f32 v[6:7], v[90:91], v[22:23], v[112:113]
	v_pk_mul_f32 v[22:23], v[36:37], v[24:25] op_sel_hi:[1,0]
	s_nop 0
	v_pk_fma_f32 v[8:9], v[92:93], v[22:23], v[114:115]
	v_pk_mul_f32 v[22:23], v[58:59], v[24:25] op_sel_hi:[1,0]
	s_nop 0
	v_pk_fma_f32 v[2:3], v[108:109], v[22:23], v[116:117]
	v_pk_mul_f32 v[22:23], v[66:67], v[24:25] op_sel_hi:[1,0]
	s_nop 0
	v_pk_fma_f32 v[4:5], v[110:111], v[22:23], v[118:119]
	v_cndmask_b32_e64 v22, 0, 1, s[40:41]
	v_cmp_ne_u32_e64 s[38:39], 1, v22
	s_cbranch_vccnz .LBB0_1357
	s_mov_b64 s[58:59], 0
	global_store_dwordx4 v[20:21], v[6:9], off
	global_store_dwordx4 v[20:21], v[2:5], off offset:16

.LBB0_1359:
	v_mov_b32_e32 v25, v24
	v_pk_mul_f32 v[38:39], v[38:39], v[24:25]
	v_pk_mul_f32 v[40:41], v[40:41], v[24:25]
	v_pk_mul_f32 v[42:43], v[42:43], v[24:25]
	v_pk_mul_f32 v[44:45], v[44:45], v[24:25]
	s_and_b64 vcc, exec, s[38:39]
	s_mov_b64 s[56:57], -1
	s_waitcnt vmcnt(10)
	v_pk_fma_f32 v[6:7], v[38:39], v[120:121], v[128:129]
	v_pk_fma_f32 v[8:9], v[40:41], v[122:123], v[130:131]
	v_pk_fma_f32 v[2:3], v[42:43], v[124:125], v[132:133]
	v_pk_fma_f32 v[4:5], v[44:45], v[126:127], v[134:135]
	s_cbranch_vccnz .LBB0_1361
	s_mov_b64 s[56:57], 0
	global_store_dwordx4 v[20:21], v[6:9], off offset:2048
	global_store_dwordx4 v[20:21], v[2:5], off offset:2064

.LBB0_1363:
	s_nop 0
	s_nop 0
	s_nop 0
	v_pk_mul_f32 v[30:31], v[30:31], v[24:25]
	v_pk_mul_f32 v[32:33], v[32:33], v[24:25]
	v_pk_mul_f32 v[26:27], v[26:27], v[24:25]
	v_pk_mul_f32 v[28:29], v[28:29], v[24:25]
	s_and_b64 vcc, exec, s[38:39]
	s_mov_b64 s[56:57], -1
	s_waitcnt vmcnt(8)
	v_pk_fma_f32 v[6:7], v[30:31], v[136:137], v[144:145]
	v_pk_fma_f32 v[8:9], v[32:33], v[138:139], v[146:147]
	v_pk_fma_f32 v[2:3], v[26:27], v[140:141], v[148:149]
	v_pk_fma_f32 v[4:5], v[28:29], v[142:143], v[150:151]
	s_cbranch_vccnz .LBB0_1365
	v_add_co_u32_e32 v26, vcc, 0x1000, v20
	s_mov_b64 s[56:57], 0
	s_nop 0
	v_addc_co_u32_e32 v27, vcc, 0, v21, vcc
	global_store_dwordx4 v[26:27], v[6:9], off
	global_store_dwordx4 v[26:27], v[2:5], off offset:16

.LBB0_1367:
	s_mov_b64 s[56:57], 0x1800
	s_nop 0
	s_nop 0
	s_nop 0
	v_pk_mul_f32 v[16:17], v[16:17], v[24:25]
	v_pk_mul_f32 v[18:19], v[18:19], v[24:25]
	v_pk_mul_f32 v[12:13], v[12:13], v[24:25]
	v_pk_mul_f32 v[14:15], v[14:15], v[24:25]
	s_and_b64 vcc, exec, s[38:39]
	s_mov_b64 s[38:39], -1
	s_waitcnt vmcnt(6)
	v_pk_fma_f32 v[6:7], v[16:17], v[152:153], v[160:161]
	v_pk_fma_f32 v[8:9], v[18:19], v[154:155], v[162:163]
	v_pk_fma_f32 v[2:3], v[12:13], v[156:157], v[164:165]
	v_pk_fma_f32 v[4:5], v[14:15], v[158:159], v[166:167]
	s_cbranch_vccnz .LBB0_1369
	v_add_co_u32_e32 v12, vcc, 0x1000, v20
	s_mov_b64 s[38:39], 0
	s_nop 0
	v_addc_co_u32_e32 v13, vcc, 0, v21, vcc
	global_store_dwordx4 v[12:13], v[6:9], off offset:2048
	global_store_dwordx4 v[12:13], v[2:5], off offset:2064
